# E11: E10 + waves 4-7 delayed by s_sleep 8 at the top of every sel far tile (stagger the two waves of each SIMD)
# baseline (speedup 1.0000x reference)
.LBB0_500:
	s_or_b64 exec, exec, s[0:1]
	v_mov_b32_e32 v2, v226
	s_waitcnt lgkmcnt(0)
	s_barrier
	s_movk_i32 s0, 0x400
	v_readfirstlane_b32 s10, v2
	s_nop 3
	s_cmpk_lt_u32 s10, 0x100
	s_cselect_b32 s32, 0, 1
	s_cbranch_scc1 .Lnsa_prio_done
	s_setprio 1

.LBB0_588:
	s_or_b64 exec, exec, s[2:3]
	v_max_f32_e32 v0, v49, v48
	v_max3_f32 v0, v0, v33, v32
	v_max3_f32 v0, v0, v35, v34
	v_max3_f32 v0, v0, v29, v28
	v_max3_f32 v0, v0, v31, v30
	v_max3_f32 v0, v0, v25, v24
	v_max3_f32 v0, v0, v27, v26
	v_max3_f32 v0, v0, v21, v20
	v_mov_b32_e32 v6, v0
	s_nop 1
	v_permlane16_swap_b32_e32 v0, v6
	v_max_f32_e32 v0, v0, v6
	v_mov_b32_e32 v6, v0
	s_nop 1
	v_permlane32_swap_b32_e32 v0, v6
	v_max3_f32 v198, v47, v0, v6
	v_sub_f32_e32 v0, v49, v198
	v_exp_f32_e32 v0, v0
	v_sub_f32_e32 v6, v48, v198
	v_exp_f32_e32 v6, v6
	v_sub_f32_e32 v7, v32, v198
	v_add_f32_e32 v0, 0, v0
	v_exp_f32_e32 v7, v7
	v_add_f32_e32 v0, v6, v0
	v_sub_f32_e32 v6, v33, v198
	v_exp_f32_e32 v6, v6
	v_sub_f32_e32 v32, v35, v198
	v_exp_f32_e32 v32, v32
	v_sub_f32_e32 v33, v34, v198
	v_exp_f32_e32 v33, v33
	v_add_f32_e32 v0, v6, v0
	v_add_f32_e32 v0, v7, v0
	v_add_f32_e32 v0, v32, v0
	v_add_f32_e32 v7, v33, v0
	v_sub_f32_e32 v0, v29, v198
	v_exp_f32_e32 v29, v0
	v_sub_f32_e32 v0, v28, v198
	v_exp_f32_e32 v33, v0
	v_sub_f32_e32 v0, v31, v198
	v_exp_f32_e32 v31, v0
	v_sub_f32_e32 v0, v30, v198
	v_exp_f32_e32 v35, v0
	v_sub_f32_e32 v0, v25, v198
	v_exp_f32_e32 v25, v0
	v_sub_f32_e32 v0, v24, v198
	v_sub_f32_e32 v48, v47, v198
	v_exp_f32_e32 v47, v0
	v_sub_f32_e32 v0, v27, v198
	v_exp_f32_e32 v27, v0
	v_sub_f32_e32 v0, v26, v198
	v_exp_f32_e32 v49, v0
	v_sub_f32_e32 v0, v21, v198
	v_exp_f32_e32 v21, v0
	v_sub_f32_e32 v0, v20, v198
	v_exp_f32_e32 v51, v0
	v_max_f32_e32 v0, v23, v22
	v_max3_f32 v0, v0, v17, v16
	v_max3_f32 v0, v0, v19, v18
	v_max3_f32 v0, v0, v13, v12
	v_max3_f32 v0, v0, v15, v14
	v_max3_f32 v0, v0, v9, v8
	v_max3_f32 v0, v0, v11, v10
	v_max3_f32 v0, v0, v5, v4
	v_mov_b32_e32 v6, v0
	s_nop 1
	v_permlane16_swap_b32_e32 v0, v6
	v_max_f32_e32 v0, v0, v6
	v_mov_b32_e32 v6, v0
	s_nop 1
	v_permlane32_swap_b32_e32 v0, v6
	v_max3_f32 v199, v46, v0, v6
	v_sub_f32_e32 v0, v23, v199
	v_exp_f32_e32 v0, v0
	v_sub_f32_e32 v6, v22, v199
	v_exp_f32_e32 v6, v6
	v_sub_f32_e32 v16, v16, v199
	v_add_f32_e32 v0, 0, v0
	v_exp_f32_e32 v16, v16
	v_add_f32_e32 v0, v6, v0
	v_sub_f32_e32 v6, v17, v199
	v_exp_f32_e32 v6, v6
	v_sub_f32_e32 v17, v19, v199
	v_exp_f32_e32 v17, v17
	v_sub_f32_e32 v18, v18, v199
	v_exp_f32_e32 v18, v18
	v_add_f32_e32 v0, v6, v0
	v_add_f32_e32 v0, v16, v0
	v_add_f32_e32 v0, v17, v0
	v_add_f32_e32 v6, v18, v0
	v_sub_f32_e32 v0, v13, v199
	v_exp_f32_e32 v28, v0
	v_sub_f32_e32 v0, v12, v199
	v_exp_f32_e32 v32, v0
	v_sub_f32_e32 v0, v15, v199
	v_exp_f32_e32 v30, v0
	v_sub_f32_e32 v0, v14, v199
	v_exp_f32_e32 v34, v0
	v_sub_f32_e32 v0, v9, v199
	v_exp_f32_e32 v24, v0
	v_sub_f32_e32 v0, v8, v199
	v_sub_f32_e32 v22, v46, v199
	v_exp_f32_e32 v46, v0
	v_sub_f32_e32 v0, v11, v199
	v_exp_f32_e32 v26, v0
	v_sub_f32_e32 v0, v10, v199
	v_exp_f32_e32 v23, v48
	v_exp_f32_e32 v48, v0
	v_sub_f32_e32 v0, v5, v199
	v_exp_f32_e32 v20, v0
	v_sub_f32_e32 v0, v4, v199
	v_pk_add_f32 v[4:5], v[28:29], v[6:7]
	v_exp_f32_e32 v50, v0
	v_pk_add_f32 v[4:5], v[32:33], v[4:5]
	v_exp_f32_e32 v22, v22
	v_pk_add_f32 v[4:5], v[30:31], v[4:5]
	s_waitcnt vmcnt(0)
	s_addk_i32 s0, 0xfc00
	v_pk_add_f32 v[4:5], v[34:35], v[4:5]
	s_add_i32 s2, s96, s0
	v_pk_add_f32 v[4:5], v[24:25], v[4:5]
	s_add_i32 s1, s1, 1
	v_pk_add_f32 v[4:5], v[46:47], v[4:5]
	v_lshl_add_u64 v[42:43], v[42:43], 0, s[12:13]
	v_pk_add_f32 v[4:5], v[26:27], v[4:5]
	s_cmp_lg_u32 s2, 0
	v_pk_add_f32 v[4:5], v[48:49], v[4:5]
	v_lshl_add_u64 v[44:45], v[44:45], 0, s[12:13]
	v_pk_add_f32 v[4:5], v[20:21], v[4:5]
	s_waitcnt vmcnt(0)
	v_pk_add_f32 v[4:5], v[50:51], v[4:5]
	s_barrier
	v_pk_fma_f32 v[40:41], v[40:41], v[22:23], v[4:5]
	s_cbranch_scc1 .LBB0_520
	v_mov_b32_e32 v0, v41
	s_nop 1
	v_permlane16_swap_b32_e32 v41, v0
	v_add_f32_e32 v5, v41, v0
	v_mov_b32_e32 v0, v40
	s_nop 1
	v_permlane16_swap_b32_e32 v40, v0
	v_add_f32_e32 v4, v40, v0
	v_mov_b32_e32 v7, v5
	v_mov_b32_e32 v6, v4
	s_nop 0
	v_permlane32_swap_b32_e32 v5, v7
	v_permlane32_swap_b32_e32 v4, v6
	v_pk_add_f32 v[6:7], v[4:5], v[6:7]
	s_mov_b32 m0, s28
	v_div_scale_f32 v0, s[0:1], v7, v7, 1.0
	v_rcp_f32_e32 v4, v0
	v_readlane_b32 s0, v253, 8
	s_add_u32 s0, s0, s37
	v_readlane_b32 s1, v253, 10
	v_fma_f32 v5, -v0, v4, 1.0
	v_fmac_f32_e32 v4, v5, v4
	v_div_scale_f32 v5, vcc, 1.0, v7, 1.0
	v_mul_f32_e32 v8, v5, v4
	v_fma_f32 v9, -v0, v8, v5
	v_fmac_f32_e32 v8, v9, v4
	v_fma_f32 v0, -v0, v8, v5
	v_div_scale_f32 v5, s[2:3], v6, v6, 1.0
	v_div_fmas_f32 v0, v0, v4, v8
	v_rcp_f32_e32 v8, v5
	v_div_fixup_f32 v0, v0, v7, 1.0
	v_cmp_lt_f32_e32 vcc, 0, v7
	s_addc_u32 s1, s1, 0
	global_load_lds_dwordx4 v[36:37], off
	v_cndmask_b32_e32 v100, 0, v0, vcc
	v_fma_f32 v0, -v5, v8, 1.0
	v_fmac_f32_e32 v8, v0, v8
	v_div_scale_f32 v0, vcc, 1.0, v6, 1.0
	v_mul_f32_e32 v7, v0, v8
	v_fma_f32 v9, -v5, v7, v0
	v_fmac_f32_e32 v7, v9, v8
	v_fma_f32 v0, -v5, v7, v0
	s_mov_b32 m0, s81
	v_div_fmas_f32 v0, v0, v8, v7
	global_load_lds_dwordx4 v[38:39], off
	v_lshl_add_u64 v[8:9], s[0:1], 0, v[104:105]
	s_mov_b32 m0, s77
	v_div_fixup_f32 v0, v0, v6, 1.0
	global_load_lds_dwordx4 v[8:9], off
	v_lshl_add_u64 v[8:9], s[0:1], 0, v[110:111]
	s_mov_b32 m0, s78
	v_cmp_lt_f32_e32 vcc, 0, v6
	global_load_lds_dwordx4 v[8:9], off
	s_waitcnt vmcnt(0)
	v_mov_b32_e32 v4, 0
	v_cndmask_b32_e32 v128, 0, v0, vcc
	v_mov_b32_e32 v129, v128
	v_mov_b32_e32 v101, v100
	s_mov_b32 s2, 0
	v_mov_b32_e32 v200, v154
	v_mov_b32_e32 v201, v153
	v_mov_b64_e32 v[130:131], v[116:117]
	v_mov_b64_e32 v[132:133], v[118:119]
	v_mov_b64_e32 v[134:135], v[122:123]
	v_mov_b64_e32 v[136:137], v[120:121]
	s_mov_b32 s3, 0
	v_mov_b32_e32 v5, v4
	v_mov_b32_e32 v6, v4
	v_mov_b32_e32 v7, v4
	v_mov_b32_e32 v8, v4
	v_mov_b32_e32 v9, v4
	v_mov_b32_e32 v10, v4
	v_mov_b32_e32 v11, v4
	v_mov_b32_e32 v12, v4
	v_mov_b32_e32 v13, v4
	v_mov_b32_e32 v14, v4
	v_mov_b32_e32 v15, v4
	v_mov_b32_e32 v16, v4
	v_mov_b32_e32 v17, v4
	v_mov_b32_e32 v18, v4
	v_mov_b32_e32 v19, v4
	v_mov_b32_e32 v20, v4
	v_mov_b32_e32 v21, v4
	v_mov_b32_e32 v22, v4
	v_mov_b32_e32 v23, v4
	v_mov_b32_e32 v24, v4
	v_mov_b32_e32 v25, v4
	v_mov_b32_e32 v26, v4
	v_mov_b32_e32 v27, v4
	v_mov_b32_e32 v28, v4
	v_mov_b32_e32 v29, v4
	v_mov_b32_e32 v30, v4
	v_mov_b32_e32 v31, v4
	v_mov_b32_e32 v32, v4
	v_mov_b32_e32 v33, v4
	v_mov_b32_e32 v34, v4
	v_mov_b32_e32 v35, v4
	v_mov_b32_e32 v36, v4
	v_mov_b32_e32 v37, v4
	v_mov_b32_e32 v38, v4
	v_mov_b32_e32 v39, v4
	v_mov_b32_e32 v40, v4
	v_mov_b32_e32 v41, v4
	v_mov_b32_e32 v42, v4
	v_mov_b32_e32 v43, v4
	v_mov_b32_e32 v44, v4
	v_mov_b32_e32 v45, v4
	v_mov_b32_e32 v46, v4
	v_mov_b32_e32 v47, v4
	v_mov_b32_e32 v48, v4
	v_mov_b32_e32 v49, v4
	v_mov_b32_e32 v50, v4
	v_mov_b32_e32 v51, v4
	v_mov_b32_e32 v52, v4
	v_mov_b32_e32 v53, v4
	v_mov_b32_e32 v54, v4
	v_mov_b32_e32 v55, v4
	v_mov_b32_e32 v56, v4
	v_mov_b32_e32 v57, v4
	v_mov_b32_e32 v58, v4
	v_mov_b32_e32 v59, v4
	v_mov_b32_e32 v60, v4
	v_mov_b32_e32 v61, v4
	v_mov_b32_e32 v62, v4
	v_mov_b32_e32 v63, v4
	v_mov_b32_e32 v64, v4
	v_mov_b32_e32 v65, v4
	v_mov_b32_e32 v66, v4
	v_mov_b32_e32 v67, v4
	s_waitcnt vmcnt(0) lgkmcnt(0)
	s_barrier
	s_branch .LBB0_591
	s_nop 0
	s_nop 0
	s_nop 0
	s_nop 0
	s_nop 0
	s_nop 0
	s_nop 0
	s_nop 0
	s_nop 0
	s_nop 0
	s_nop 0
	s_nop 0
	s_nop 0
	s_nop 0
	s_nop 0
	s_nop 0
	s_nop 0
	s_nop 0
	s_nop 0
	s_nop 0
	s_nop 0
	s_nop 0
	s_nop 0
	s_nop 0
	s_nop 0
	s_nop 0
	s_nop 0
	s_nop 0
	s_nop 0

.LBB0_687:
	s_cmp_eq_u32 s32, 0
	s_cbranch_scc1 .Lst687
	s_sleep 8

.LBB0_700:
	s_lshl_b32 s8, s36, 19
	s_cmp_gt_i32 s82, s86
	s_cbranch_scc1 .LBB0_781
	s_sub_i32 s36, s2, s43
	s_sub_i32 s84, 0, s42
	s_cmp_ge_i32 s82, s42
	s_mov_b64 s[0:1], -1
	s_cbranch_scc0 .LBB0_704
	s_branch .LBB0_703
	s_nop 0
	s_nop 0
	s_nop 0
	s_nop 0
	s_nop 0
	s_nop 0
	s_nop 0
	s_nop 0
	s_nop 0
	s_nop 0
	s_nop 0
	s_nop 0
	s_nop 0
	s_nop 0
	s_nop 0
	s_nop 0
	s_nop 0
	s_nop 0
	s_nop 0
	s_nop 0
	s_nop 0
	s_nop 0
	s_nop 0
	s_nop 0
	s_nop 0
	s_nop 0
	s_nop 0
	s_nop 0
	s_nop 0
	s_nop 0
	s_nop 0
	s_nop 0
	s_nop 0
	s_nop 0
	s_nop 0
	s_nop 0
	s_nop 0
